# stack + router: DPP/permlane-swap butterfly sums instead of ds_bpermute, rows prefetched two tokens ahead, loop-end wait counts only the next row
# baseline (speedup 1.0000x reference)
.LBB0_1247:
	s_ashr_i32 s63, s62, 31
	s_lshl_b64 s[64:65], s[62:63], 8
	s_add_u32 s40, s64, s12
	s_addc_u32 s41, s65, s13
	s_lshl_b64 s[0:1], s[40:41], 11
	v_lshl_add_u64 v[114:115], v[156:157], 0, s[0:1]
	global_load_dwordx4 v[126:129], v[114:115], off
	global_load_dwordx4 v[122:125], v[114:115], off offset:1024
	global_load_dwordx4 v[240:243], v[114:115], off offset:2048
	global_load_dwordx4 v[244:247], v[114:115], off offset:3072
	v_mov_b32_e32 v239, 0
	v_mov_b32_e32 v167, 0
	s_and_saveexec_b64 s[42:43], s[2:3]
	s_cbranch_execz .LBB0_1249
	s_lshl_b64 s[0:1], s[40:41], 6
	v_lshl_add_u64 v[114:115], v[132:133], 0, s[0:1]
	global_load_dword v167, v[114:115], off
	global_load_dword v239, v[114:115], off offset:64

.LBB0_1250:
	s_or_b64 exec, exec, s[70:71]
	s_add_i32 s0, s0, 4
	s_add_u32 s68, s68, 4
	s_addc_u32 s69, s69, 0
	s_add_u32 s66, s66, 8
	s_mov_b64 s[28:29], 0x400
	s_addc_u32 s67, s67, 0
	v_lshl_add_u64 v[164:165], v[164:165], 0, s[28:29]
	s_mov_b64 s[28:29], 0x800
	v_lshl_add_u64 v[162:163], v[162:163], 0, 64
	v_lshl_add_u64 v[160:161], v[160:161], 0, s[28:29]
	s_waitcnt vmcnt(11)
	s_bitcmp1_b32 s0, 2
	s_cbranch_scc1 .Lrt_cp_l1
	v_mov_b64_e32 v[128:129], v[120:121]
	v_mov_b64_e32 v[124:125], v[116:117]
	v_mov_b64_e32 v[126:127], v[118:119]
	v_mov_b64_e32 v[122:123], v[114:115]
	v_mov_b32_e32 v167, v195
	s_branch .Lrt_cp_done
.Lrt_cp_l1:
	v_mov_b64_e32 v[128:129], v[242:243]
	v_mov_b64_e32 v[124:125], v[246:247]
	v_mov_b64_e32 v[126:127], v[240:241]
	v_mov_b64_e32 v[122:123], v[244:245]
	v_mov_b32_e32 v167, v239
.Lrt_cp_done:
	s_cmpk_eq_i32 s0, 0x80
	s_cbranch_scc1 .LBB0_1257
.LBB0_1251:
	s_bitcmp1_b32 s0, 2
	s_cbranch_scc1 .Lrt_ld_l1
	v_readlane_b32 s28, v249, 5
	v_readlane_b32 s29, v249, 6
	v_mov_b32_e32 v195, 0
	s_nop 0
	v_lshl_add_u64 v[218:219], s[28:29], 0, v[160:161]
	v_add_co_u32_e32 v218, vcc, 0xdf00800, v218
	s_nop 1
	v_addc_co_u32_e32 v219, vcc, 0, v219, vcc
	global_load_dwordx4 v[118:121], v[218:219], off offset:2048
	global_load_dwordx4 v[114:117], v[218:219], off offset:3072
	s_and_saveexec_b64 s[40:41], s[2:3]
	v_lshl_add_u64 v[168:169], s[28:29], 0, v[162:163]
	global_load_dword v195, v[168:169], off offset:64
	s_or_b64 exec, exec, s[40:41]
	s_branch .LBB0_1255
.Lrt_ld_l1:
	v_readlane_b32 s28, v249, 5
	v_readlane_b32 s29, v249, 6
	v_mov_b32_e32 v239, 0
	s_nop 0
	v_lshl_add_u64 v[218:219], s[28:29], 0, v[160:161]
	v_add_co_u32_e32 v218, vcc, 0xdf00800, v218
	s_nop 1
	v_addc_co_u32_e32 v219, vcc, 0, v219, vcc
	global_load_dwordx4 v[240:243], v[218:219], off offset:2048
	global_load_dwordx4 v[244:247], v[218:219], off offset:3072
	s_and_saveexec_b64 s[40:41], s[2:3]
	v_lshl_add_u64 v[168:169], s[28:29], 0, v[162:163]
	global_load_dword v239, v[168:169], off offset:64
	s_or_b64 exec, exec, s[40:41]
.LBB0_1255:
	v_lshlrev_b32_e32 v172, 16, v126
	v_and_b32_e32 v178, 0xffff0000, v126
	v_lshlrev_b32_e32 v186, 16, v127
	v_and_b32_e32 v188, 0xffff0000, v127
	v_lshlrev_b32_e32 v166, 16, v128
	v_and_b32_e32 v170, 0xffff0000, v128
	v_lshlrev_b32_e32 v182, 16, v129
	v_and_b32_e32 v184, 0xffff0000, v129
	v_lshlrev_b32_e32 v126, 16, v122
	v_and_b32_e32 v128, 0xffff0000, v122
	v_lshlrev_b32_e32 v176, 16, v123
	v_and_b32_e32 v180, 0xffff0000, v123
	v_lshlrev_b32_e32 v122, 16, v124
	v_and_b32_e32 v124, 0xffff0000, v124
	v_lshlrev_b32_e32 v168, 16, v125
	v_and_b32_e32 v174, 0xffff0000, v125
	v_pk_fma_f32 v[190:191], v[172:173], v[140:141], 0 op_sel_hi:[0,1,0]
	v_pk_fma_f32 v[190:191], v[178:179], v[2:3], v[190:191] op_sel_hi:[0,1,1]
	v_pk_fma_f32 v[190:191], v[186:187], v[142:143], v[190:191] op_sel_hi:[0,1,1]
	v_pk_fma_f32 v[190:191], v[188:189], v[4:5], v[190:191] op_sel_hi:[0,1,1]
	v_pk_fma_f32 v[190:191], v[166:167], v[144:145], v[190:191] op_sel_hi:[0,1,1]
	v_pk_fma_f32 v[190:191], v[170:171], v[6:7], v[190:191] op_sel_hi:[0,1,1]
	v_pk_fma_f32 v[190:191], v[182:183], v[146:147], v[190:191] op_sel_hi:[0,1,1]
	v_pk_fma_f32 v[190:191], v[184:185], v[8:9], v[190:191] op_sel_hi:[0,1,1]
	v_pk_fma_f32 v[190:191], v[126:127], v[148:149], v[190:191] op_sel_hi:[0,1,1]
	v_pk_fma_f32 v[190:191], v[128:129], v[10:11], v[190:191] op_sel_hi:[0,1,1]
	v_pk_fma_f32 v[190:191], v[176:177], v[150:151], v[190:191] op_sel_hi:[0,1,1]
	v_pk_fma_f32 v[190:191], v[180:181], v[12:13], v[190:191] op_sel_hi:[0,1,1]
	v_pk_fma_f32 v[190:191], v[122:123], v[152:153], v[190:191] op_sel_hi:[0,1,1]
	v_pk_fma_f32 v[190:191], v[124:125], v[14:15], v[190:191] op_sel_hi:[0,1,1]
	v_pk_fma_f32 v[190:191], v[168:169], v[154:155], v[190:191] op_sel_hi:[0,1,1]
	v_pk_fma_f32 v[190:191], v[174:175], v[16:17], v[190:191] op_sel_hi:[0,1,1]
	v_fma_f32 v224, v172, v22, 0
	v_fma_f32 v225, v172, v46, 0
	v_fma_f32 v226, v172, v50, 0
	v_fma_f32 v227, v172, v66, 0
	v_fma_f32 v228, v172, v86, 0
	v_fma_f32 v229, v172, v102, 0
	v_fmac_f32_e32 v224, v178, v23
	v_fmac_f32_e32 v225, v178, v47
	v_fmac_f32_e32 v226, v178, v51
	v_fmac_f32_e32 v227, v178, v67
	v_fmac_f32_e32 v228, v178, v87
	v_fmac_f32_e32 v229, v178, v103
	v_fmac_f32_e32 v224, v186, v24
	v_fmac_f32_e32 v225, v186, v48
	v_fmac_f32_e32 v226, v186, v52
	v_fmac_f32_e32 v227, v186, v68
	v_fmac_f32_e32 v228, v186, v88
	v_fmac_f32_e32 v229, v186, v104
	v_fmac_f32_e32 v224, v188, v25
	v_fmac_f32_e32 v225, v188, v49
	v_fmac_f32_e32 v226, v188, v53
	v_fmac_f32_e32 v227, v188, v69
	v_fmac_f32_e32 v228, v188, v89
	v_fmac_f32_e32 v229, v188, v105
	v_fmac_f32_e32 v224, v166, v18
	v_fmac_f32_e32 v225, v166, v34
	v_fmac_f32_e32 v226, v166, v54
	v_fmac_f32_e32 v227, v166, v70
	v_fmac_f32_e32 v228, v166, v82
	v_fmac_f32_e32 v229, v166, v98
	v_fmac_f32_e32 v224, v170, v19
	v_fmac_f32_e32 v225, v170, v35
	v_fmac_f32_e32 v226, v170, v55
	v_fmac_f32_e32 v227, v170, v71
	v_fmac_f32_e32 v228, v170, v83
	v_fmac_f32_e32 v229, v170, v99
	v_fmac_f32_e32 v224, v182, v20
	v_fmac_f32_e32 v225, v182, v36
	v_fmac_f32_e32 v226, v182, v56
	v_fmac_f32_e32 v227, v182, v72
	v_fmac_f32_e32 v228, v182, v84
	v_fmac_f32_e32 v229, v182, v100
	v_fmac_f32_e32 v224, v184, v21
	v_fmac_f32_e32 v225, v184, v37
	v_fmac_f32_e32 v226, v184, v57
	v_fmac_f32_e32 v227, v184, v73
	v_fmac_f32_e32 v228, v184, v85
	v_fmac_f32_e32 v229, v184, v101
	v_fmac_f32_e32 v224, v126, v26
	v_fmac_f32_e32 v225, v126, v38
	v_fmac_f32_e32 v226, v126, v62
	v_fmac_f32_e32 v227, v126, v74
	v_fmac_f32_e32 v228, v126, v90
	v_fmac_f32_e32 v229, v126, v106
	v_fmac_f32_e32 v224, v128, v27
	v_fmac_f32_e32 v225, v128, v39
	v_fmac_f32_e32 v226, v128, v63
	v_fmac_f32_e32 v227, v128, v75
	v_fmac_f32_e32 v228, v128, v91
	v_fmac_f32_e32 v229, v128, v107
	v_fmac_f32_e32 v224, v176, v28
	v_fmac_f32_e32 v225, v176, v40
	v_fmac_f32_e32 v226, v176, v64
	v_fmac_f32_e32 v227, v176, v76
	v_fmac_f32_e32 v228, v176, v92
	v_fmac_f32_e32 v229, v176, v108
	v_fmac_f32_e32 v224, v180, v29
	v_fmac_f32_e32 v225, v180, v41
	v_fmac_f32_e32 v226, v180, v65
	v_fmac_f32_e32 v227, v180, v77
	v_fmac_f32_e32 v228, v180, v93
	v_fmac_f32_e32 v229, v180, v109
	v_fmac_f32_e32 v224, v122, v30
	v_fmac_f32_e32 v225, v122, v42
	v_fmac_f32_e32 v226, v122, v58
	v_fmac_f32_e32 v227, v122, v78
	v_fmac_f32_e32 v228, v122, v94
	v_fmac_f32_e32 v229, v122, v110
	v_fmac_f32_e32 v224, v124, v31
	v_fmac_f32_e32 v225, v124, v43
	v_fmac_f32_e32 v226, v124, v59
	v_fmac_f32_e32 v227, v124, v79
	v_fmac_f32_e32 v228, v124, v95
	v_fmac_f32_e32 v229, v124, v111
	v_fmac_f32_e32 v224, v168, v32
	v_fmac_f32_e32 v225, v168, v44
	v_fmac_f32_e32 v226, v168, v60
	v_fmac_f32_e32 v227, v168, v80
	v_fmac_f32_e32 v228, v168, v96
	v_fmac_f32_e32 v229, v168, v112
	v_fmac_f32_e32 v224, v174, v33
	v_fmac_f32_e32 v225, v174, v45
	v_fmac_f32_e32 v226, v174, v61
	v_fmac_f32_e32 v227, v174, v81
	v_fmac_f32_e32 v228, v174, v97
	v_fmac_f32_e32 v229, v174, v113
	s_nop 1
	v_add_f32_dpp v190, v190, v190 quad_perm:[1,0,3,2] row_mask:0xf bank_mask:0xf
	v_add_f32_dpp v191, v191, v191 quad_perm:[1,0,3,2] row_mask:0xf bank_mask:0xf
	v_add_f32_dpp v224, v224, v224 quad_perm:[1,0,3,2] row_mask:0xf bank_mask:0xf
	v_add_f32_dpp v225, v225, v225 quad_perm:[1,0,3,2] row_mask:0xf bank_mask:0xf
	v_add_f32_dpp v226, v226, v226 quad_perm:[1,0,3,2] row_mask:0xf bank_mask:0xf
	v_add_f32_dpp v227, v227, v227 quad_perm:[1,0,3,2] row_mask:0xf bank_mask:0xf
	v_add_f32_dpp v228, v228, v228 quad_perm:[1,0,3,2] row_mask:0xf bank_mask:0xf
	v_add_f32_dpp v229, v229, v229 quad_perm:[1,0,3,2] row_mask:0xf bank_mask:0xf
	v_add_f32_dpp v167, v167, v167 quad_perm:[1,0,3,2] row_mask:0xf bank_mask:0xf
	v_add_f32_dpp v190, v190, v190 quad_perm:[2,3,0,1] row_mask:0xf bank_mask:0xf
	v_add_f32_dpp v191, v191, v191 quad_perm:[2,3,0,1] row_mask:0xf bank_mask:0xf
	v_add_f32_dpp v224, v224, v224 quad_perm:[2,3,0,1] row_mask:0xf bank_mask:0xf
	v_add_f32_dpp v225, v225, v225 quad_perm:[2,3,0,1] row_mask:0xf bank_mask:0xf
	v_add_f32_dpp v226, v226, v226 quad_perm:[2,3,0,1] row_mask:0xf bank_mask:0xf
	v_add_f32_dpp v227, v227, v227 quad_perm:[2,3,0,1] row_mask:0xf bank_mask:0xf
	v_add_f32_dpp v228, v228, v228 quad_perm:[2,3,0,1] row_mask:0xf bank_mask:0xf
	v_add_f32_dpp v229, v229, v229 quad_perm:[2,3,0,1] row_mask:0xf bank_mask:0xf
	v_add_f32_dpp v167, v167, v167 quad_perm:[2,3,0,1] row_mask:0xf bank_mask:0xf
	v_add_f32_dpp v190, v190, v190 row_half_mirror row_mask:0xf bank_mask:0xf
	v_add_f32_dpp v191, v191, v191 row_half_mirror row_mask:0xf bank_mask:0xf
	v_add_f32_dpp v224, v224, v224 row_half_mirror row_mask:0xf bank_mask:0xf
	v_add_f32_dpp v225, v225, v225 row_half_mirror row_mask:0xf bank_mask:0xf
	v_add_f32_dpp v226, v226, v226 row_half_mirror row_mask:0xf bank_mask:0xf
	v_add_f32_dpp v227, v227, v227 row_half_mirror row_mask:0xf bank_mask:0xf
	v_add_f32_dpp v228, v228, v228 row_half_mirror row_mask:0xf bank_mask:0xf
	v_add_f32_dpp v229, v229, v229 row_half_mirror row_mask:0xf bank_mask:0xf
	v_add_f32_dpp v167, v167, v167 row_half_mirror row_mask:0xf bank_mask:0xf
	v_add_f32_dpp v190, v190, v190 row_mirror row_mask:0xf bank_mask:0xf
	v_add_f32_dpp v191, v191, v191 row_mirror row_mask:0xf bank_mask:0xf
	v_add_f32_dpp v224, v224, v224 row_mirror row_mask:0xf bank_mask:0xf
	v_add_f32_dpp v225, v225, v225 row_mirror row_mask:0xf bank_mask:0xf
	v_add_f32_dpp v226, v226, v226 row_mirror row_mask:0xf bank_mask:0xf
	v_add_f32_dpp v227, v227, v227 row_mirror row_mask:0xf bank_mask:0xf
	v_add_f32_dpp v228, v228, v228 row_mirror row_mask:0xf bank_mask:0xf
	v_add_f32_dpp v229, v229, v229 row_mirror row_mask:0xf bank_mask:0xf
	v_add_f32_dpp v167, v167, v167 row_mirror row_mask:0xf bank_mask:0xf
	v_mov_b32_e32 v230, v190
	v_mov_b32_e32 v231, v191
	v_mov_b32_e32 v232, v224
	v_mov_b32_e32 v233, v225
	v_mov_b32_e32 v234, v226
	v_mov_b32_e32 v235, v227
	v_mov_b32_e32 v236, v228
	v_mov_b32_e32 v237, v229
	v_mov_b32_e32 v238, v167
	v_permlane16_swap_b32_e32 v190, v230
	v_permlane16_swap_b32_e32 v191, v231
	v_permlane16_swap_b32_e32 v224, v232
	v_permlane16_swap_b32_e32 v225, v233
	v_permlane16_swap_b32_e32 v226, v234
	v_permlane16_swap_b32_e32 v227, v235
	v_permlane16_swap_b32_e32 v228, v236
	v_permlane16_swap_b32_e32 v229, v237
	v_permlane16_swap_b32_e32 v167, v238
	v_add_f32_e32 v190, v190, v230
	v_add_f32_e32 v191, v191, v231
	v_add_f32_e32 v224, v224, v232
	v_add_f32_e32 v225, v225, v233
	v_add_f32_e32 v226, v226, v234
	v_add_f32_e32 v227, v227, v235
	v_add_f32_e32 v228, v228, v236
	v_add_f32_e32 v229, v229, v237
	v_add_f32_e32 v167, v167, v238
	v_mov_b32_e32 v230, v190
	v_mov_b32_e32 v231, v191
	v_mov_b32_e32 v232, v224
	v_mov_b32_e32 v233, v225
	v_mov_b32_e32 v234, v226
	v_mov_b32_e32 v235, v227
	v_mov_b32_e32 v236, v228
	v_mov_b32_e32 v237, v229
	v_mov_b32_e32 v238, v167
	v_permlane32_swap_b32_e32 v190, v230
	v_permlane32_swap_b32_e32 v191, v231
	v_permlane32_swap_b32_e32 v224, v232
	v_permlane32_swap_b32_e32 v225, v233
	v_permlane32_swap_b32_e32 v226, v234
	v_permlane32_swap_b32_e32 v227, v235
	v_permlane32_swap_b32_e32 v228, v236
	v_permlane32_swap_b32_e32 v229, v237
	v_permlane32_swap_b32_e32 v167, v238
	v_add_f32_e32 v190, v190, v230
	v_add_f32_e32 v191, v191, v231
	v_add_f32_e32 v224, v224, v232
	v_add_f32_e32 v225, v225, v233
	v_add_f32_e32 v226, v226, v234
	v_add_f32_e32 v227, v227, v235
	v_add_f32_e32 v228, v228, v236
	v_add_f32_e32 v229, v229, v237
	v_add_f32_e32 v167, v167, v238
	v_fmamk_f32 v167, v167, 0x3a800000, v204
	v_mul_f32_e32 v173, 0x4f800000, v167
	v_cmp_gt_f32_e32 vcc, s15, v167
	s_nop 1
	v_cndmask_b32_e32 v167, v167, v173, vcc
	v_sqrt_f32_e32 v173, v167
	s_nop 0
	v_add_u32_e32 v169, -1, v173
	v_fma_f32 v177, -v169, v173, v167
	v_cmp_ge_f32_e64 s[40:41], 0, v177
	v_add_u32_e32 v177, 1, v173
	s_nop 0
	v_cndmask_b32_e64 v169, v173, v169, s[40:41]
	v_fma_f32 v173, -v177, v173, v167
	v_cmp_lt_f32_e64 s[40:41], 0, v173
	s_nop 1
	v_cndmask_b32_e64 v169, v169, v177, s[40:41]
	v_mul_f32_e32 v173, 0x37800000, v169
	v_cndmask_b32_e32 v169, v169, v173, vcc
	v_cmp_class_f32_e32 vcc, v167, v205
	s_nop 1
	v_cndmask_b32_e32 v167, v169, v167, vcc
	v_div_scale_f32 v169, s[28:29], v167, v167, 1.0
	v_rcp_f32_e32 v173, v169
	s_nop 0
	v_fma_f32 v123, -v169, v173, 1.0
	v_fmac_f32_e32 v173, v123, v173
	v_div_scale_f32 v123, vcc, 1.0, v167, 1.0
	v_mul_f32_e32 v127, v123, v173
	v_fma_f32 v177, -v169, v127, v123
	v_fmac_f32_e32 v127, v177, v173
	v_fma_f32 v123, -v169, v127, v123
	v_div_fmas_f32 v123, v123, v173, v127
	v_div_fixup_f32 v202, v123, v167, 1.0
	v_mul_f32_e32 v210, 0x3e000000, v202
	v_mov_b32_e32 v187, v188
	v_mov_b32_e32 v173, v178
	v_mov_b32_e32 v183, v184
	v_mov_b32_e32 v167, v170
	v_mov_b32_e32 v177, v180
	v_mov_b32_e32 v127, v128
	v_mov_b32_e32 v169, v174
	v_mov_b32_e32 v123, v124
	v_pk_mul_f32 v[186:187], v[210:211], v[186:187] op_sel_hi:[0,1]
	v_pk_mul_f32 v[172:173], v[210:211], v[172:173] op_sel_hi:[0,1]
	v_pk_mul_f32 v[182:183], v[210:211], v[182:183] op_sel_hi:[0,1]
	v_pk_mul_f32 v[166:167], v[210:211], v[166:167] op_sel_hi:[0,1]
	v_pk_mul_f32 v[176:177], v[210:211], v[176:177] op_sel_hi:[0,1]
	v_pk_mul_f32 v[126:127], v[210:211], v[126:127] op_sel_hi:[0,1]
	v_pk_mul_f32 v[168:169], v[210:211], v[168:169] op_sel_hi:[0,1]
	v_pk_mul_f32 v[122:123], v[210:211], v[122:123] op_sel_hi:[0,1]
	v_mov_b32_e32 v210, v203
	v_mov_b32_e32 v211, v203
	v_cvt_pk_fp8_f32 v210, v172, v173
	v_cvt_pk_fp8_f32 v211, v166, v167
	v_mov_b32_e32 v166, v203
	v_mov_b32_e32 v167, v203
	v_cvt_pk_fp8_f32 v166, v126, v127
	v_cvt_pk_fp8_f32 v167, v122, v123
	v_readlane_b32 s28, v249, 5
	v_cvt_pk_fp8_f32 v210, v186, v187 op_sel:[0,0,1]
	v_cvt_pk_fp8_f32 v211, v182, v183 op_sel:[0,0,1]
	v_readlane_b32 s29, v249, 6
	v_cvt_pk_fp8_f32 v166, v176, v177 op_sel:[0,0,1]
	v_cvt_pk_fp8_f32 v167, v168, v169 op_sel:[0,0,1]
	v_lshl_add_u64 v[122:123], s[28:29], 0, v[164:165]
	v_add_co_u32_e32 v122, vcc, 0x28600000, v122
	s_nop 1
	v_addc_co_u32_e32 v123, vcc, 0, v123, vcc
	global_store_dwordx2 v[122:123], v[210:211], off
	global_store_dwordx2 v[122:123], v[166:167], off offset:512
	s_and_saveexec_b64 s[70:71], s[4:5]
	s_cbranch_execz .LBB0_1250
	v_mov_b32_e32 v122, v190
	v_mov_b32_e32 v123, v191
	v_mov_b32_e32 v125, v224
	v_cmp_gt_f32_e32 vcc, v122, v123
	v_mov_b32_e32 v166, v225
	v_mov_b32_e32 v128, v226
	v_cndmask_b32_e32 v129, v123, v122, vcc
	v_cmp_gt_f32_e64 s[40:41], v125, v129
	v_mov_b32_e32 v127, v227
	v_cndmask_b32_e64 v167, 0, 1, vcc
	v_cndmask_b32_e64 v129, v129, v125, s[40:41]
	v_cmp_gt_f32_e64 s[42:43], v166, v129
	v_cndmask_b32_e64 v167, v167, 2, s[40:41]
	v_mov_b32_e32 v126, v228
	v_cndmask_b32_e64 v129, v129, v166, s[42:43]
	v_cmp_gt_f32_e64 s[44:45], v128, v129
	v_cndmask_b32_e64 v167, v167, 3, s[42:43]
	v_mov_b32_e32 v124, v229
	v_cndmask_b32_e64 v129, v129, v128, s[44:45]
	v_cmp_gt_f32_e64 s[46:47], v127, v129
	v_cndmask_b32_e64 v167, v167, 4, s[44:45]
	s_mov_b32 s1, 0xff800000
	v_cndmask_b32_e64 v129, v129, v127, s[46:47]
	v_cmp_gt_f32_e64 s[48:49], v126, v129
	v_cndmask_b32_e64 v167, v167, 5, s[46:47]
	v_cmp_nlg_f32_e64 s[52:53], s1, v123
	v_cndmask_b32_e64 v129, v129, v126, s[48:49]
	v_cndmask_b32_e64 v167, v167, 6, s[48:49]
	v_cmp_ngt_f32_e32 vcc, v124, v129
	s_and_b64 s[28:29], vcc, s[48:49]
	s_add_i32 s1, s17, s0
	v_cndmask_b32_e32 v167, 7, v167, vcc
	v_cmp_eq_u32_e64 s[50:51], 0, v167
	s_or_b64 s[50:51], s[50:51], s[52:53]
	v_cmp_ne_u32_e64 s[48:49], 1, v167
	v_cndmask_b32_e64 v123, v123, v216, s[50:51]
	v_cmp_gt_f32_e64 s[52:53], v122, v123
	s_and_b64 s[48:49], s[48:49], s[52:53]
	v_cndmask_b32_e64 v122, v123, v122, s[48:49]
	v_cmp_ne_u32_e64 s[46:47], 2, v167
	v_cmp_gt_f32_e64 s[52:53], v125, v122
	s_and_b64 s[46:47], s[46:47], s[52:53]
	v_cndmask_b32_e64 v122, v122, v125, s[46:47]
	v_cmp_ne_u32_e64 s[44:45], 3, v167
	v_cmp_gt_f32_e64 s[52:53], v166, v122
	s_and_b64 s[44:45], s[44:45], s[52:53]
	v_cndmask_b32_e64 v122, v122, v166, s[44:45]
	v_cmp_ne_u32_e64 s[42:43], 4, v167
	v_cmp_gt_f32_e64 s[52:53], v128, v122
	s_and_b64 s[42:43], s[42:43], s[52:53]
	v_cndmask_b32_e64 v122, v122, v128, s[42:43]
	v_cmp_ne_u32_e64 s[40:41], 5, v167
	v_cmp_gt_f32_e64 s[52:53], v127, v122
	s_and_b64 s[40:41], s[40:41], s[52:53]
	v_cndmask_b32_e64 v122, v122, v127, s[40:41]
	v_cmp_ngt_f32_e64 s[52:53], v126, v122
	s_or_b64 s[52:53], s[28:29], s[52:53]
	v_cndmask_b32_e32 v123, v124, v129, vcc
	v_cndmask_b32_e64 v122, v126, v122, s[52:53]
	v_cmp_gt_f32_e64 s[54:55], v124, v122
	s_and_b64 s[54:55], vcc, s[54:55]
	v_cndmask_b32_e64 v125, 0, -1, s[50:51]
	v_cndmask_b32_e64 v122, v122, v124, s[54:55]
	v_sub_f32_e32 v122, v122, v123
	v_mul_f32_e32 v122, v202, v122
	v_mul_f32_e32 v122, 0x3fb8aa3b, v122
	v_exp_f32_e32 v122, v122
	v_readlane_b32 s34, v249, 5
	v_readlane_b32 s35, v249, 6
	v_add_f32_e32 v122, 1.0, v122
	v_div_scale_f32 v123, s[28:29], v122, v122, 1.0
	v_rcp_f32_e32 v124, v123
	s_add_u32 s28, s34, s68
	s_addc_u32 s29, s35, s69
	v_fma_f32 v126, -v123, v124, 1.0
	v_fmac_f32_e32 v124, v126, v124
	v_div_scale_f32 v126, vcc, 1.0, v122, 1.0
	v_mul_f32_e32 v127, v126, v124
	v_fma_f32 v128, -v123, v127, v126
	v_fmac_f32_e32 v127, v128, v124
	v_fma_f32 v123, -v123, v127, v126
	v_div_fmas_f32 v123, v123, v124, v127
	v_lshlrev_b32_e32 v124, 8, v125
	v_mov_b32_e32 v125, 0x100
	v_cndmask_b32_e64 v124, v124, v125, s[48:49]
	v_mov_b32_e32 v125, 0x200
	v_cndmask_b32_e64 v124, v124, v125, s[46:47]
	v_mov_b32_e32 v125, 0x300
	v_cndmask_b32_e64 v124, v124, v125, s[44:45]
	v_mov_b32_e32 v125, 0x400
	v_cndmask_b32_e64 v124, v124, v125, s[42:43]
	v_mov_b32_e32 v125, 0x500
	v_cndmask_b32_e64 v124, v124, v125, s[40:41]
	v_mov_b32_e32 v125, 0x600
	v_cndmask_b32_e64 v124, v125, v124, s[52:53]
	v_mov_b32_e32 v125, 0x700
	v_cndmask_b32_e64 v124, v124, v125, s[54:55]
	v_add_u32_e32 v124, v124, v167
	global_store_dword v203, v124, s[28:29]
	s_add_u32 s28, s34, s66
	v_div_fixup_f32 v122, v123, v122, 1.0
	s_addc_u32 s29, s35, s67
	v_readlane_b32 s34, v255, 46
	v_sub_f32_e32 v123, 1.0, v122
	v_mov_b32_e32 v125, s1
	v_readlane_b32 s35, v255, 47
	ds_write_b32 v125, v124
	global_store_dwordx2 v203, v[122:123], s[28:29]
	s_branch .LBB0_1250
.LBB0_1257:
	s_waitcnt vmcnt(0)
	v_mov_b32_e32 v114, 0
	s_waitcnt lgkmcnt(0)
	s_barrier
	s_and_saveexec_b64 s[54:55], s[6:7]
	s_cbranch_execz .LBB0_1308
	ds_read_b32 v114, v189
	s_waitcnt lgkmcnt(0)
	v_cmp_eq_u32_sdwa s[42:43], v114, v203 src0_sel:BYTE_0 src1_sel:DWORD
	s_and_saveexec_b64 s[40:41], s[4:5]
	s_bcnt1_i32_b64 s0, s[42:43]
	s_add_i32 s1, s17, s18
	v_mov_b32_e32 v115, s1
	v_mov_b32_e32 v116, s0
	ds_write_b32 v115, v116 offset:1024
	s_or_b64 exec, exec, s[40:41]
	v_cmp_eq_u32_sdwa s[42:43], v114, v217 src0_sel:BYTE_0 src1_sel:DWORD
	s_and_saveexec_b64 s[40:41], s[4:5]
	s_bcnt1_i32_b64 s0, s[42:43]
	s_add_i32 s1, s17, s18
	v_mov_b32_e32 v115, s1
	v_mov_b32_e32 v116, s0
	ds_write_b32 v115, v116 offset:1040
	s_or_b64 exec, exec, s[40:41]
	v_mov_b32_e32 v115, 2
	v_cmp_eq_u32_sdwa s[42:43], v114, v115 src0_sel:BYTE_0 src1_sel:DWORD
	s_and_saveexec_b64 s[40:41], s[4:5]
	s_bcnt1_i32_b64 s0, s[42:43]
	s_add_i32 s1, s17, s18
	v_mov_b32_e32 v115, s1
	v_mov_b32_e32 v116, s0
	ds_write_b32 v115, v116 offset:1056
	s_or_b64 exec, exec, s[40:41]
	v_mov_b32_e32 v115, 3
	v_cmp_eq_u32_sdwa s[42:43], v114, v115 src0_sel:BYTE_0 src1_sel:DWORD
	s_and_saveexec_b64 s[40:41], s[4:5]
	s_bcnt1_i32_b64 s0, s[42:43]
	s_add_i32 s1, s17, s18
	v_mov_b32_e32 v115, s1
	v_mov_b32_e32 v116, s0
	ds_write_b32 v115, v116 offset:1072
	s_or_b64 exec, exec, s[40:41]
	v_mov_b32_e32 v115, 4
	v_cmp_eq_u32_sdwa s[42:43], v114, v115 src0_sel:BYTE_0 src1_sel:DWORD
	s_and_saveexec_b64 s[40:41], s[4:5]
	s_bcnt1_i32_b64 s0, s[42:43]
	s_add_i32 s1, s17, s18
	v_mov_b32_e32 v115, s1
	v_mov_b32_e32 v116, s0
	ds_write_b32 v115, v116 offset:1088
	s_or_b64 exec, exec, s[40:41]
	v_mov_b32_e32 v115, 5
	v_cmp_eq_u32_sdwa s[42:43], v114, v115 src0_sel:BYTE_0 src1_sel:DWORD
	s_and_saveexec_b64 s[40:41], s[4:5]
	s_bcnt1_i32_b64 s0, s[42:43]
	s_add_i32 s1, s17, s18
	v_mov_b32_e32 v115, s1
	v_mov_b32_e32 v116, s0
	ds_write_b32 v115, v116 offset:1104
	s_or_b64 exec, exec, s[40:41]
	v_mov_b32_e32 v115, 6
	v_cmp_eq_u32_sdwa s[42:43], v114, v115 src0_sel:BYTE_0 src1_sel:DWORD
	s_and_saveexec_b64 s[40:41], s[4:5]
	s_bcnt1_i32_b64 s0, s[42:43]
	s_add_i32 s1, s17, s18
	v_mov_b32_e32 v115, s1
	v_mov_b32_e32 v116, s0
	ds_write_b32 v115, v116 offset:1120
	s_or_b64 exec, exec, s[40:41]
	v_cmp_eq_u32_sdwa s[42:43], v114, v222 src0_sel:BYTE_0 src1_sel:DWORD
	s_and_saveexec_b64 s[40:41], s[4:5]
	s_bcnt1_i32_b64 s0, s[42:43]
	s_add_i32 s1, s17, s18
	v_mov_b32_e32 v115, s1
	v_mov_b32_e32 v116, s0
	ds_write_b32 v115, v116 offset:1136
	s_or_b64 exec, exec, s[40:41]
	v_ashrrev_i32_e32 v115, 8, v114
	v_cmp_eq_u32_sdwa s[42:43], v115, v203 src0_sel:BYTE_0 src1_sel:DWORD
	s_and_saveexec_b64 s[40:41], s[4:5]
	s_bcnt1_i32_b64 s0, s[42:43]
	s_add_i32 s1, s17, s18
	v_mov_b32_e32 v116, s1
	v_mov_b32_e32 v117, s0
	ds_write_b32 v116, v117 offset:1152
	s_or_b64 exec, exec, s[40:41]
	v_cmp_eq_u32_sdwa s[42:43], v115, v217 src0_sel:BYTE_0 src1_sel:DWORD
	s_and_saveexec_b64 s[40:41], s[4:5]
	s_bcnt1_i32_b64 s0, s[42:43]
	s_add_i32 s1, s17, s18
	v_mov_b32_e32 v116, s1
	v_mov_b32_e32 v117, s0
	ds_write_b32 v116, v117 offset:1168
	s_or_b64 exec, exec, s[40:41]
	v_mov_b32_e32 v116, 2
	v_cmp_eq_u32_sdwa s[42:43], v115, v116 src0_sel:BYTE_0 src1_sel:DWORD
	s_and_saveexec_b64 s[40:41], s[4:5]
	s_bcnt1_i32_b64 s0, s[42:43]
	s_add_i32 s1, s17, s18
	v_mov_b32_e32 v116, s1
	v_mov_b32_e32 v117, s0
	ds_write_b32 v116, v117 offset:1184
	s_or_b64 exec, exec, s[40:41]
	v_mov_b32_e32 v116, 3
	v_cmp_eq_u32_sdwa s[42:43], v115, v116 src0_sel:BYTE_0 src1_sel:DWORD
	s_and_saveexec_b64 s[40:41], s[4:5]
	s_bcnt1_i32_b64 s0, s[42:43]
	s_add_i32 s1, s17, s18
	v_mov_b32_e32 v116, s1
	v_mov_b32_e32 v117, s0
	ds_write_b32 v116, v117 offset:1200
	s_or_b64 exec, exec, s[40:41]
	v_mov_b32_e32 v116, 4
	v_cmp_eq_u32_sdwa s[42:43], v115, v116 src0_sel:BYTE_0 src1_sel:DWORD
	s_and_saveexec_b64 s[40:41], s[4:5]
	s_bcnt1_i32_b64 s0, s[42:43]
	s_add_i32 s1, s17, s18
	v_mov_b32_e32 v116, s1
	v_mov_b32_e32 v117, s0
	ds_write_b32 v116, v117 offset:1216
	s_or_b64 exec, exec, s[40:41]
	v_mov_b32_e32 v116, 5
	v_cmp_eq_u32_sdwa s[42:43], v115, v116 src0_sel:BYTE_0 src1_sel:DWORD
	s_and_saveexec_b64 s[40:41], s[4:5]
	s_bcnt1_i32_b64 s0, s[42:43]
	s_add_i32 s1, s17, s18
	v_mov_b32_e32 v116, s1
	v_mov_b32_e32 v117, s0
	ds_write_b32 v116, v117 offset:1232
	s_or_b64 exec, exec, s[40:41]
	v_mov_b32_e32 v116, 6
	v_cmp_eq_u32_sdwa s[42:43], v115, v116 src0_sel:BYTE_0 src1_sel:DWORD
	s_and_saveexec_b64 s[40:41], s[4:5]
	s_bcnt1_i32_b64 s0, s[42:43]
	s_add_i32 s1, s17, s18
	v_mov_b32_e32 v116, s1
	v_mov_b32_e32 v117, s0
	ds_write_b32 v116, v117 offset:1248
	s_or_b64 exec, exec, s[40:41]
	v_cmp_eq_u32_sdwa s[42:43], v115, v222 src0_sel:BYTE_0 src1_sel:DWORD
	s_and_saveexec_b64 s[40:41], s[4:5]
	s_bcnt1_i32_b64 s0, s[42:43]
	s_add_i32 s1, s17, s18
	v_mov_b32_e32 v116, s1
	v_mov_b32_e32 v117, s0
	ds_write_b32 v116, v117 offset:1264
	s_or_b64 exec, exec, s[40:41]
	v_lshlrev_b32_e32 v114, 3, v114
	v_and_b32_e32 v114, 0x7f8, v114
	v_add_u32_e32 v115, v114, v115
	v_mov_b32_e32 v114, 0
	s_mov_b32 s0, 0
	v_mov_b32_e32 v116, v115
	s_mov_b32 s1, s21
	s_branch .LBB0_1292
